# grid barrier release path: the completing XCD leader invalidates, bumps the top word and every XCD's generation word itself and waits only for the invalidate; other leaders no longer bump their XCD wo
# speedup vs baseline: 1.0244x; 1.0021x over previous
.LBB0_165:
	s_or_b64 exec, exec, s[10:11]
	v_cvt_f32_u32_e32 v4, v1
	s_waitcnt vmcnt(0)
	v_readfirstlane_b32 s2, v3
	s_add_u32 s10, s76, 0x3500
	s_addc_u32 s11, s77, 0
	v_rcp_iflag_f32_e32 v4, v4
	v_add_u32_e32 v2, s2, v2
	v_add_u32_e32 v5, 1, v2
	s_mov_b64 s[12:13], -1
	v_mul_f32_e32 v3, 0x4f7ffffe, v4
	v_cvt_u32_f32_e32 v3, v3
	v_sub_u32_e32 v4, 0, v1
	v_mul_lo_u32 v4, v4, v3
	v_mul_hi_u32 v4, v3, v4
	v_add_u32_e32 v3, v3, v4
	v_mul_hi_u32 v3, v2, v3
	v_mul_lo_u32 v4, v3, v1
	v_sub_u32_e32 v2, v2, v4
	v_add_u32_e32 v6, 1, v3
	v_cmp_ge_u32_e32 vcc, v2, v1
	v_sub_u32_e32 v4, v2, v1
	s_nop 0
	v_cndmask_b32_e32 v3, v3, v6, vcc
	v_cndmask_b32_e32 v2, v2, v4, vcc
	v_add_u32_e32 v4, 1, v3
	v_cmp_ge_u32_e32 vcc, v2, v1
	s_nop 1
	v_cndmask_b32_e32 v4, v3, v4, vcc
	v_mul_lo_u32 v2, v1, v4
	v_add_u32_e32 v1, v2, v1
	v_cmp_ne_u32_e32 vcc, v5, v1
	v_mov_b64_e32 v[2:3], s[10:11]
	s_mov_b64 s[98:99], vcc
	s_and_saveexec_b64 s[8:9], vcc
	s_cbranch_execz .LBB0_177
	v_mov_b32_e32 v1, 0
	global_load_dword v2, v1, s[10:11] sc1
	s_mov_b64 s[16:17], 0
	s_waitcnt vmcnt(0)
	v_cmp_eq_u32_e32 vcc, v2, v4
	s_and_saveexec_b64 s[14:15], vcc
	s_cbranch_execz .LBB0_176
	s_add_u32 s12, s76, 0x200
	s_addc_u32 s13, s77, 0
	s_mov_b32 s2, 1
	s_branch .LBB0_169

.LBB0_177:
	s_or_b64 exec, exec, s[8:9]
	buffer_inv sc1
	s_and_saveexec_b64 s[8:9], s[12:13]
	s_cbranch_execz .LBB0_179
	v_mov_b32_e32 v1, 1
	global_atomic_add v[2:3], v1, off
.LBB0_179:
	s_or_b64 exec, exec, s[8:9]
	s_and_b64 vcc, exec, s[98:99]
	s_cbranch_vccnz .Lbar_nl1
	v_mov_b32_e32 v1, 0x2400
	v_mov_b32_e32 v2, 1
	global_atomic_add v1, v2, s[76:77]
	global_atomic_add v1, v2, s[76:77] offset:256
	global_atomic_add v1, v2, s[76:77] offset:512
	global_atomic_add v1, v2, s[76:77] offset:768
	global_atomic_add v1, v2, s[76:77] offset:1024
	global_atomic_add v1, v2, s[76:77] offset:1280
	global_atomic_add v1, v2, s[76:77] offset:1536
	global_atomic_add v1, v2, s[76:77] offset:1792
	global_atomic_add v1, v2, s[76:77] offset:2048
	global_atomic_add v1, v2, s[76:77] offset:2304
	global_atomic_add v1, v2, s[76:77] offset:2560
	global_atomic_add v1, v2, s[76:77] offset:2816
	global_atomic_add v1, v2, s[76:77] offset:3072
	global_atomic_add v1, v2, s[76:77] offset:3328
	global_atomic_add v1, v2, s[76:77] offset:3584
	global_atomic_add v1, v2, s[76:77] offset:3840
	s_waitcnt vmcnt(17)
	s_branch .Lbar_dn1

.Lbar_dn1:
.LBB0_180:
	s_or_b64 exec, exec, s[0:1]
	s_waitcnt lgkmcnt(0)
	s_barrier

.LBB0_303:
	s_or_b64 exec, exec, s[8:9]
	v_cvt_f32_u32_e32 v4, v1
	s_waitcnt vmcnt(0)
	v_readfirstlane_b32 s2, v3
	s_add_u32 s8, s76, 0x3500
	s_addc_u32 s9, s77, 0
	v_rcp_iflag_f32_e32 v4, v4
	v_add_u32_e32 v2, s2, v2
	v_add_u32_e32 v5, 1, v2
	s_mov_b64 s[10:11], -1
	v_mul_f32_e32 v3, 0x4f7ffffe, v4
	v_cvt_u32_f32_e32 v3, v3
	v_sub_u32_e32 v4, 0, v1
	v_mul_lo_u32 v4, v4, v3
	v_mul_hi_u32 v4, v3, v4
	v_add_u32_e32 v3, v3, v4
	v_mul_hi_u32 v3, v2, v3
	v_mul_lo_u32 v4, v3, v1
	v_sub_u32_e32 v2, v2, v4
	v_add_u32_e32 v6, 1, v3
	v_cmp_ge_u32_e32 vcc, v2, v1
	v_sub_u32_e32 v4, v2, v1
	s_nop 0
	v_cndmask_b32_e32 v3, v3, v6, vcc
	v_cndmask_b32_e32 v2, v2, v4, vcc
	v_add_u32_e32 v4, 1, v3
	v_cmp_ge_u32_e32 vcc, v2, v1
	s_nop 1
	v_cndmask_b32_e32 v4, v3, v4, vcc
	v_mul_lo_u32 v2, v1, v4
	v_add_u32_e32 v1, v2, v1
	v_cmp_ne_u32_e32 vcc, v5, v1
	v_mov_b64_e32 v[2:3], s[8:9]
	s_mov_b64 s[98:99], vcc
	s_and_saveexec_b64 s[6:7], vcc
	s_cbranch_execz .LBB0_315
	v_mov_b32_e32 v1, 0
	global_load_dword v2, v1, s[8:9] sc1
	s_mov_b64 s[14:15], 0
	s_waitcnt vmcnt(0)
	v_cmp_eq_u32_e32 vcc, v2, v4
	s_and_saveexec_b64 s[12:13], vcc
	s_cbranch_execz .LBB0_314
	s_add_u32 s10, s76, 0x200
	s_addc_u32 s11, s77, 0
	s_mov_b32 s2, 1
	s_branch .LBB0_307

.LBB0_315:
	s_or_b64 exec, exec, s[6:7]
	buffer_inv sc1
	s_and_saveexec_b64 s[6:7], s[10:11]
	s_cbranch_execz .LBB0_317
	v_mov_b32_e32 v1, 1
	global_atomic_add v[2:3], v1, off
.LBB0_317:
	s_or_b64 exec, exec, s[6:7]
	s_and_b64 vcc, exec, s[98:99]
	s_cbranch_vccnz .Lbar_nl2
	v_mov_b32_e32 v1, 0x2400
	v_mov_b32_e32 v2, 1
	global_atomic_add v1, v2, s[76:77]
	global_atomic_add v1, v2, s[76:77] offset:256
	global_atomic_add v1, v2, s[76:77] offset:512
	global_atomic_add v1, v2, s[76:77] offset:768
	global_atomic_add v1, v2, s[76:77] offset:1024
	global_atomic_add v1, v2, s[76:77] offset:1280
	global_atomic_add v1, v2, s[76:77] offset:1536
	global_atomic_add v1, v2, s[76:77] offset:1792
	global_atomic_add v1, v2, s[76:77] offset:2048
	global_atomic_add v1, v2, s[76:77] offset:2304
	global_atomic_add v1, v2, s[76:77] offset:2560
	global_atomic_add v1, v2, s[76:77] offset:2816
	global_atomic_add v1, v2, s[76:77] offset:3072
	global_atomic_add v1, v2, s[76:77] offset:3328
	global_atomic_add v1, v2, s[76:77] offset:3584
	global_atomic_add v1, v2, s[76:77] offset:3840
	s_waitcnt vmcnt(17)
	s_branch .Lbar_dn2

.LBB0_1052:
	s_or_b64 exec, exec, s[12:13]
	v_cvt_f32_u32_e32 v4, v1
	s_waitcnt vmcnt(0)
	v_readfirstlane_b32 s10, v3
	s_add_u32 s12, s76, 0x3500
	s_addc_u32 s13, s77, 0
	v_rcp_iflag_f32_e32 v4, v4
	v_add_u32_e32 v2, s10, v2
	v_add_u32_e32 v5, 1, v2
	s_mov_b64 s[14:15], -1
	v_mul_f32_e32 v3, 0x4f7ffffe, v4
	v_cvt_u32_f32_e32 v3, v3
	v_sub_u32_e32 v4, 0, v1
	v_mul_lo_u32 v4, v4, v3
	v_mul_hi_u32 v4, v3, v4
	v_add_u32_e32 v3, v3, v4
	v_mul_hi_u32 v3, v2, v3
	v_mul_lo_u32 v4, v3, v1
	v_sub_u32_e32 v2, v2, v4
	v_add_u32_e32 v6, 1, v3
	v_cmp_ge_u32_e32 vcc, v2, v1
	v_sub_u32_e32 v4, v2, v1
	s_nop 0
	v_cndmask_b32_e32 v3, v3, v6, vcc
	v_cndmask_b32_e32 v2, v2, v4, vcc
	v_add_u32_e32 v4, 1, v3
	v_cmp_ge_u32_e32 vcc, v2, v1
	s_nop 1
	v_cndmask_b32_e32 v4, v3, v4, vcc
	v_mul_lo_u32 v2, v1, v4
	v_add_u32_e32 v1, v2, v1
	v_cmp_ne_u32_e32 vcc, v5, v1
	v_mov_b64_e32 v[2:3], s[12:13]
	s_mov_b64 s[98:99], vcc
	s_and_saveexec_b64 s[10:11], vcc
	s_cbranch_execz .LBB0_1064
	v_mov_b32_e32 v1, 0
	global_load_dword v2, v1, s[12:13] sc1
	s_mov_b64 s[18:19], 0
	s_waitcnt vmcnt(0)
	v_cmp_eq_u32_e32 vcc, v2, v4
	s_and_saveexec_b64 s[16:17], vcc
	s_cbranch_execz .LBB0_1063
	s_add_u32 s14, s76, 0x200
	s_addc_u32 s15, s77, 0
	s_mov_b32 s28, 1
	s_branch .LBB0_1056

.LBB0_1064:
	s_or_b64 exec, exec, s[10:11]
	buffer_inv sc1
	s_and_saveexec_b64 s[10:11], s[14:15]
	s_cbranch_execz .LBB0_1066
	v_mov_b32_e32 v1, 1
	global_atomic_add v[2:3], v1, off
.LBB0_1066:
	s_or_b64 exec, exec, s[10:11]
	s_and_b64 vcc, exec, s[98:99]
	s_cbranch_vccnz .Lbar_nl4
	v_mov_b32_e32 v1, 0x2400
	v_mov_b32_e32 v2, 1
	global_atomic_add v1, v2, s[76:77]
	global_atomic_add v1, v2, s[76:77] offset:256
	global_atomic_add v1, v2, s[76:77] offset:512
	global_atomic_add v1, v2, s[76:77] offset:768
	global_atomic_add v1, v2, s[76:77] offset:1024
	global_atomic_add v1, v2, s[76:77] offset:1280
	global_atomic_add v1, v2, s[76:77] offset:1536
	global_atomic_add v1, v2, s[76:77] offset:1792
	global_atomic_add v1, v2, s[76:77] offset:2048
	global_atomic_add v1, v2, s[76:77] offset:2304
	global_atomic_add v1, v2, s[76:77] offset:2560
	global_atomic_add v1, v2, s[76:77] offset:2816
	global_atomic_add v1, v2, s[76:77] offset:3072
	global_atomic_add v1, v2, s[76:77] offset:3328
	global_atomic_add v1, v2, s[76:77] offset:3584
	global_atomic_add v1, v2, s[76:77] offset:3840
	s_waitcnt vmcnt(17)
	s_branch .Lbar_dn4

.LBB0_1161:
	s_or_b64 exec, exec, s[10:11]
	v_cvt_f32_u32_e32 v4, v1
	s_waitcnt vmcnt(0)
	v_readfirstlane_b32 s8, v3
	s_add_u32 s10, s76, 0x3500
	s_addc_u32 s11, s77, 0
	v_rcp_iflag_f32_e32 v4, v4
	v_add_u32_e32 v2, s8, v2
	v_add_u32_e32 v5, 1, v2
	s_mov_b64 s[12:13], -1
	v_mul_f32_e32 v3, 0x4f7ffffe, v4
	v_cvt_u32_f32_e32 v3, v3
	v_sub_u32_e32 v4, 0, v1
	v_mul_lo_u32 v4, v4, v3
	v_mul_hi_u32 v4, v3, v4
	v_add_u32_e32 v3, v3, v4
	v_mul_hi_u32 v3, v2, v3
	v_mul_lo_u32 v4, v3, v1
	v_sub_u32_e32 v2, v2, v4
	v_add_u32_e32 v6, 1, v3
	v_cmp_ge_u32_e32 vcc, v2, v1
	v_sub_u32_e32 v4, v2, v1
	s_nop 0
	v_cndmask_b32_e32 v3, v3, v6, vcc
	v_cndmask_b32_e32 v2, v2, v4, vcc
	v_add_u32_e32 v4, 1, v3
	v_cmp_ge_u32_e32 vcc, v2, v1
	s_nop 1
	v_cndmask_b32_e32 v4, v3, v4, vcc
	v_mul_lo_u32 v2, v1, v4
	v_add_u32_e32 v1, v2, v1
	v_cmp_ne_u32_e32 vcc, v5, v1
	v_mov_b64_e32 v[2:3], s[10:11]
	s_mov_b64 s[98:99], vcc
	s_and_saveexec_b64 s[8:9], vcc
	s_cbranch_execz .LBB0_1173
	v_mov_b32_e32 v1, 0
	global_load_dword v2, v1, s[10:11] sc1
	s_mov_b64 s[16:17], 0
	s_waitcnt vmcnt(0)
	v_cmp_eq_u32_e32 vcc, v2, v4
	s_and_saveexec_b64 s[14:15], vcc
	s_cbranch_execz .LBB0_1172
	s_add_u32 s12, s76, 0x200
	s_addc_u32 s13, s77, 0
	s_mov_b32 s26, 1
	s_branch .LBB0_1165

.Lbar_dn8:
.LBB0_1423:
	s_or_b64 exec, exec, s[2:3]
	s_waitcnt lgkmcnt(0)
	s_barrier
